# speedup vs baseline: 1.0009x; 1.0009x over previous
.Lk_144:
	v_or_b32_e32 v46, 0x400, v54
	buffer_load_dwordx4 v[46:49], v46, s[4:7], 0 offen sc1
	ds_read_b128 v[50:53], v1
	v_mov_b32_e32 v66, 0
	v_add_u32_e32 v63, 0x800, v54
	s_mov_b32 s9, 0
	v_mov_b32_e32 v67, 0
	v_mov_b32_e32 v68, 0
	v_mov_b32_e32 v62, 0xc038aa3b
	s_mov_b32 s8, 0x4038aa3b
	v_mov_b32_e32 v65, 0
	v_mov_b32_e32 v64, v66
	s_setprio 3
	v_mov_b32_e32 v92, 0xc038aa3b
	v_mov_b32_e32 v93, 0xc038aa3b
	s_mov_b32 s8, 0x4038aa3b
	s_mov_b32 s9, 0
	v_mov_b32_e32 v64, 0
	v_mov_b32_e32 v65, 0
	v_mov_b32_e32 v66, 0
	v_mov_b32_e32 v67, 0
	v_mov_b32_e32 v68, 0
	v_mov_b32_e32 v116, v1
	v_mov_b32_e32 v117, v63
	s_mov_b32 s12, 0
	s_waitcnt lgkmcnt(0)
	s_setprio 3
	v_mfma_f32_16x16x32_f16 v[84:87], v[6:9], v[50:53], v[18:21]
	v_mfma_f32_16x16x32_f16 v[88:91], v[10:13], v[50:53], v[38:41]
	ds_read_b128 v[56:59], v75 offset:2048
	ds_read_b128 v[60:63], v75 offset:3072
	s_waitcnt vmcnt(1)
	v_mfma_f32_16x16x32_f16 v[84:87], v[2:5], v[42:45], v[84:87]
	v_mfma_f32_16x16x32_f16 v[88:91], v[14:17], v[42:45], v[88:91]
	s_waitcnt lgkmcnt(1)
	v_mfma_f32_16x16x32_f16 v[84:87], v[30:33], v[56:59], v[84:87]
	v_mfma_f32_16x16x32_f16 v[88:91], v[22:25], v[56:59], v[88:91]
	s_waitcnt lgkmcnt(0)
	v_mfma_f32_16x16x32_f16 v[84:87], v[34:37], v[60:63], v[84:87]
	v_mfma_f32_16x16x32_f16 v[88:91], v[26:29], v[60:63], v[88:91]
	s_nop 7
	s_setprio 0
	v_exp_f32_e32 v94, v86
	v_exp_f32_e32 v95, v90
	v_exp_f32_e32 v96, v84
	v_exp_f32_e32 v97, v88
	v_exp_f32_e32 v98, v85
	v_exp_f32_e32 v99, v89
	v_pk_add_f32 v[100:101], v[94:95], 1.0 op_sel_hi:[1,0]
	v_pk_fma_f32 v[102:103], v[94:95], s[8:9], v[92:93] op_sel_hi:[1,0,0]
	v_pk_fma_f32 v[100:101], v[96:97], v[100:101], v[100:101]
	v_pk_fma_f32 v[104:105], v[100:101], v[98:99], v[100:101]
	v_rcp_f32_e32 v104, v104
	v_rcp_f32_e32 v105, v105
	v_pk_fma_f32 v[102:103], v[102:103], v[98:99], v[102:103]
	v_pk_fma_f32 v[102:103], v[64:65], v[100:101], v[102:103]
	v_exp_f32_e32 v106, v87
	v_pk_mul_f32 v[64:65], v[102:103], v[104:105]
	v_exp_f32_e32 v108, v64
	v_exp_f32_e32 v109, v65
	v_exp_f32_e32 v107, v91
	v_pk_add_f32 v[110:111], v[108:109], 1.0 op_sel_hi:[1,0]
	v_pk_fma_f32 v[110:111], v[110:111], v[106:107], v[110:111]
	v_rcp_f32_e32 v110, v110
	v_rcp_f32_e32 v111, v111
	v_pk_add_f32 v[112:113], v[108:109], -1.0 op_sel_hi:[1,0]
	v_pk_mul_f32 v[112:113], v[112:113], v[110:111]
	v_cvt_pk_f16_f32 v114, v112, v113
	ds_write_b32 v81, v114 offset:0
	s_waitcnt lgkmcnt(0)
	global_load_dword v67, v66, s[0:1] sc1
	global_load_dword v68, v66, s[0:1] offset:4 sc1
	s_add_u32 s13, s12, 3
	s_min_u32 s13, s13, 450
	s_cmp_ge_u32 s14, s13
	s_cbranch_scc0 .Lca_slow_3
.Lca_ok_1:
	buffer_load_dwordx4 v[42:45], v117, s[4:7], 0 offen offset:0 sc1
	ds_read_b128 v[50:53], v116 offset:256
	s_setprio 0
	s_waitcnt vmcnt(3) lgkmcnt(0)
	s_setprio 3
	s_barrier
	v_mfma_f32_16x16x32_f16 v[84:87], v[6:9], v[50:53], v[18:21]
	v_mfma_f32_16x16x32_f16 v[88:91], v[10:13], v[50:53], v[38:41]
	ds_read_b128 v[56:59], v75 offset:0
	ds_read_b128 v[60:63], v75 offset:1024
	v_mfma_f32_16x16x32_f16 v[84:87], v[2:5], v[46:49], v[84:87]
	v_mfma_f32_16x16x32_f16 v[88:91], v[14:17], v[46:49], v[88:91]
	s_waitcnt lgkmcnt(1)
	v_mfma_f32_16x16x32_f16 v[84:87], v[30:33], v[56:59], v[84:87]
	v_mfma_f32_16x16x32_f16 v[88:91], v[22:25], v[56:59], v[88:91]
	s_waitcnt lgkmcnt(0)
	v_mfma_f32_16x16x32_f16 v[84:87], v[34:37], v[60:63], v[84:87]
	v_mfma_f32_16x16x32_f16 v[88:91], v[26:29], v[60:63], v[88:91]
	s_nop 7
	s_setprio 0
	v_exp_f32_e32 v94, v86
	v_exp_f32_e32 v95, v90
	v_exp_f32_e32 v96, v84
	v_exp_f32_e32 v97, v88
	v_exp_f32_e32 v98, v85
	v_exp_f32_e32 v99, v89
	v_pk_add_f32 v[100:101], v[94:95], 1.0 op_sel_hi:[1,0]
	v_pk_fma_f32 v[102:103], v[94:95], s[8:9], v[92:93] op_sel_hi:[1,0,0]
	v_pk_fma_f32 v[100:101], v[96:97], v[100:101], v[100:101]
	v_pk_fma_f32 v[104:105], v[100:101], v[98:99], v[100:101]
	v_rcp_f32_e32 v104, v104
	v_rcp_f32_e32 v105, v105
	v_pk_fma_f32 v[102:103], v[102:103], v[98:99], v[102:103]
	v_pk_fma_f32 v[102:103], v[64:65], v[100:101], v[102:103]
	v_exp_f32_e32 v106, v87
	v_pk_mul_f32 v[64:65], v[102:103], v[104:105]
	v_exp_f32_e32 v108, v64
	v_exp_f32_e32 v109, v65
	v_exp_f32_e32 v107, v91
	v_pk_add_f32 v[110:111], v[108:109], 1.0 op_sel_hi:[1,0]
	v_pk_fma_f32 v[110:111], v[110:111], v[106:107], v[110:111]
	v_rcp_f32_e32 v110, v110
	v_rcp_f32_e32 v111, v111
	v_pk_add_f32 v[112:113], v[108:109], -1.0 op_sel_hi:[1,0]
	v_pk_mul_f32 v[112:113], v[112:113], v[110:111]
	v_cvt_pk_f16_f32 v114, v112, v113
	ds_write_b32 v81, v114 offset:2048
	s_waitcnt lgkmcnt(0)
	s_add_u32 s13, s12, 4
	s_min_u32 s13, s13, 450
	s_cmp_ge_u32 s14, s13
	s_cbranch_scc0 .Lca_slow_6

.Lca_loop:
	s_setprio 3
	s_barrier
	v_mfma_f32_16x16x32_f16 v[84:87], v[6:9], v[50:53], v[18:21]
	v_mfma_f32_16x16x32_f16 v[88:91], v[10:13], v[50:53], v[38:41]
	ds_read_b128 v[56:59], v75 offset:2048
	ds_read_b128 v[60:63], v75 offset:3072
	v_mfma_f32_16x16x32_f16 v[84:87], v[2:5], v[42:45], v[84:87]
	v_mfma_f32_16x16x32_f16 v[88:91], v[14:17], v[42:45], v[88:91]
	s_waitcnt lgkmcnt(1)
	v_mfma_f32_16x16x32_f16 v[84:87], v[30:33], v[56:59], v[84:87]
	v_mfma_f32_16x16x32_f16 v[88:91], v[22:25], v[56:59], v[88:91]
	s_waitcnt lgkmcnt(0)
	v_mfma_f32_16x16x32_f16 v[84:87], v[34:37], v[60:63], v[84:87]
	v_mfma_f32_16x16x32_f16 v[88:91], v[26:29], v[60:63], v[88:91]
	s_nop 7
	s_setprio 0
	v_exp_f32_e32 v94, v86
	v_exp_f32_e32 v95, v90
	v_exp_f32_e32 v96, v84
	v_exp_f32_e32 v97, v88
	v_exp_f32_e32 v98, v85
	v_exp_f32_e32 v99, v89
	v_pk_add_f32 v[100:101], v[94:95], 1.0 op_sel_hi:[1,0]
	v_pk_fma_f32 v[102:103], v[94:95], s[8:9], v[92:93] op_sel_hi:[1,0,0]
	v_pk_fma_f32 v[100:101], v[96:97], v[100:101], v[100:101]
	v_pk_fma_f32 v[104:105], v[100:101], v[98:99], v[100:101]
	v_rcp_f32_e32 v104, v104
	v_rcp_f32_e32 v105, v105
	v_pk_fma_f32 v[102:103], v[102:103], v[98:99], v[102:103]
	v_pk_fma_f32 v[102:103], v[64:65], v[100:101], v[102:103]
	v_exp_f32_e32 v106, v87
	v_pk_mul_f32 v[64:65], v[102:103], v[104:105]
	v_exp_f32_e32 v108, v64
	v_exp_f32_e32 v109, v65
	v_exp_f32_e32 v107, v91
	v_pk_add_f32 v[110:111], v[108:109], 1.0 op_sel_hi:[1,0]
	v_pk_fma_f32 v[110:111], v[110:111], v[106:107], v[110:111]
	v_rcp_f32_e32 v110, v110
	v_rcp_f32_e32 v111, v111
	v_pk_add_f32 v[112:113], v[108:109], -1.0 op_sel_hi:[1,0]
	v_pk_mul_f32 v[112:113], v[112:113], v[110:111]
	v_cvt_pk_f16_f32 v114, v112, v113
	ds_write_b32 v81, v114 offset:0
	s_waitcnt lgkmcnt(0)
	v_min_f32_e32 v64, 0x42700000, v64
	v_min_f32_e32 v65, 0x42700000, v65
	v_readfirstlane_b32 s10, v67
	v_readfirstlane_b32 s11, v68
	global_load_dword v67, v66, s[0:1] sc1
	global_load_dword v68, v66, s[0:1] offset:4 sc1
	s_min_u32 s10, s10, s11
	s_max_u32 s14, s14, s10
	s_add_u32 s13, s12, 3
	s_min_u32 s13, s13, 450
	s_cmp_ge_u32 s14, s13
	s_cbranch_scc0 .Lca_slow_9

.Lca_ok_10:
	buffer_load_dwordx4 v[46:49], v117, s[4:7], 0 offen offset:1024 sc1
	ds_read_b128 v[50:53], v116 offset:512
	s_setprio 0
	s_waitcnt vmcnt(1) lgkmcnt(0)
	s_setprio 3
	s_barrier
	v_mfma_f32_16x16x32_f16 v[84:87], v[6:9], v[50:53], v[18:21]
	v_mfma_f32_16x16x32_f16 v[88:91], v[10:13], v[50:53], v[38:41]
	ds_read_b128 v[56:59], v75 offset:2048
	ds_read_b128 v[60:63], v75 offset:3072
	v_mfma_f32_16x16x32_f16 v[84:87], v[2:5], v[42:45], v[84:87]
	v_mfma_f32_16x16x32_f16 v[88:91], v[14:17], v[42:45], v[88:91]
	s_waitcnt lgkmcnt(1)
	v_mfma_f32_16x16x32_f16 v[84:87], v[30:33], v[56:59], v[84:87]
	v_mfma_f32_16x16x32_f16 v[88:91], v[22:25], v[56:59], v[88:91]
	s_waitcnt lgkmcnt(0)
	v_mfma_f32_16x16x32_f16 v[84:87], v[34:37], v[60:63], v[84:87]
	v_mfma_f32_16x16x32_f16 v[88:91], v[26:29], v[60:63], v[88:91]
	s_nop 7
	s_setprio 0
	v_exp_f32_e32 v94, v86
	v_exp_f32_e32 v95, v90
	v_exp_f32_e32 v96, v84
	v_exp_f32_e32 v97, v88
	v_exp_f32_e32 v98, v85
	v_exp_f32_e32 v99, v89
	v_pk_add_f32 v[100:101], v[94:95], 1.0 op_sel_hi:[1,0]
	v_pk_fma_f32 v[102:103], v[94:95], s[8:9], v[92:93] op_sel_hi:[1,0,0]
	v_pk_fma_f32 v[100:101], v[96:97], v[100:101], v[100:101]
	v_pk_fma_f32 v[104:105], v[100:101], v[98:99], v[100:101]
	v_rcp_f32_e32 v104, v104
	v_rcp_f32_e32 v105, v105
	v_pk_fma_f32 v[102:103], v[102:103], v[98:99], v[102:103]
	v_pk_fma_f32 v[102:103], v[64:65], v[100:101], v[102:103]
	v_exp_f32_e32 v106, v87
	v_pk_mul_f32 v[64:65], v[102:103], v[104:105]
	v_exp_f32_e32 v108, v64
	v_exp_f32_e32 v109, v65
	v_exp_f32_e32 v107, v91
	v_pk_add_f32 v[110:111], v[108:109], 1.0 op_sel_hi:[1,0]
	v_pk_fma_f32 v[110:111], v[110:111], v[106:107], v[110:111]
	v_rcp_f32_e32 v110, v110
	v_rcp_f32_e32 v111, v111
	v_pk_add_f32 v[112:113], v[108:109], -1.0 op_sel_hi:[1,0]
	v_pk_mul_f32 v[112:113], v[112:113], v[110:111]
	v_cvt_pk_f16_f32 v114, v112, v113
	ds_write_b32 v81, v114 offset:0
	s_waitcnt lgkmcnt(0)
	v_readfirstlane_b32 s10, v67
	v_readfirstlane_b32 s11, v68
	global_load_dword v67, v66, s[0:1] sc1
	global_load_dword v68, v66, s[0:1] offset:4 sc1
	s_min_u32 s10, s10, s11
	s_max_u32 s14, s14, s10
	s_add_u32 s13, s12, 5
	s_min_u32 s13, s13, 450
	s_cmp_ge_u32 s14, s13
	s_cbranch_scc0 .Lca_slow_15
.Lca_ok_13:
	buffer_load_dwordx4 v[42:45], v117, s[4:7], 0 offen offset:2048 sc1
	ds_read_b128 v[50:53], v116 offset:768
	s_setprio 0
	s_waitcnt vmcnt(3) lgkmcnt(0)
	s_setprio 3
	s_barrier
	v_mfma_f32_16x16x32_f16 v[84:87], v[6:9], v[50:53], v[18:21]
	v_mfma_f32_16x16x32_f16 v[88:91], v[10:13], v[50:53], v[38:41]
	ds_read_b128 v[56:59], v75 offset:0
	ds_read_b128 v[60:63], v75 offset:1024
	v_mfma_f32_16x16x32_f16 v[84:87], v[2:5], v[46:49], v[84:87]
	v_mfma_f32_16x16x32_f16 v[88:91], v[14:17], v[46:49], v[88:91]
	s_waitcnt lgkmcnt(1)
	v_mfma_f32_16x16x32_f16 v[84:87], v[30:33], v[56:59], v[84:87]
	v_mfma_f32_16x16x32_f16 v[88:91], v[22:25], v[56:59], v[88:91]
	s_waitcnt lgkmcnt(0)
	v_mfma_f32_16x16x32_f16 v[84:87], v[34:37], v[60:63], v[84:87]
	v_mfma_f32_16x16x32_f16 v[88:91], v[26:29], v[60:63], v[88:91]
	s_nop 7
	s_setprio 0
	v_exp_f32_e32 v94, v86
	v_exp_f32_e32 v95, v90
	v_exp_f32_e32 v96, v84
	v_exp_f32_e32 v97, v88
	v_exp_f32_e32 v98, v85
	v_exp_f32_e32 v99, v89
	v_pk_add_f32 v[100:101], v[94:95], 1.0 op_sel_hi:[1,0]
	v_pk_fma_f32 v[102:103], v[94:95], s[8:9], v[92:93] op_sel_hi:[1,0,0]
	v_pk_fma_f32 v[100:101], v[96:97], v[100:101], v[100:101]
	v_pk_fma_f32 v[104:105], v[100:101], v[98:99], v[100:101]
	v_rcp_f32_e32 v104, v104
	v_rcp_f32_e32 v105, v105
	v_pk_fma_f32 v[102:103], v[102:103], v[98:99], v[102:103]
	v_pk_fma_f32 v[102:103], v[64:65], v[100:101], v[102:103]
	v_exp_f32_e32 v106, v87
	v_pk_mul_f32 v[64:65], v[102:103], v[104:105]
	v_exp_f32_e32 v108, v64
	v_exp_f32_e32 v109, v65
	v_exp_f32_e32 v107, v91
	v_pk_add_f32 v[110:111], v[108:109], 1.0 op_sel_hi:[1,0]
	v_pk_fma_f32 v[110:111], v[110:111], v[106:107], v[110:111]
	v_rcp_f32_e32 v110, v110
	v_rcp_f32_e32 v111, v111
	v_pk_add_f32 v[112:113], v[108:109], -1.0 op_sel_hi:[1,0]
	v_pk_mul_f32 v[112:113], v[112:113], v[110:111]
	v_cvt_pk_f16_f32 v114, v112, v113
	ds_write_b32 v81, v114 offset:2048
	s_waitcnt lgkmcnt(0)
	s_add_u32 s13, s12, 6
	s_min_u32 s13, s13, 450
	s_cmp_ge_u32 s14, s13
	s_cbranch_scc0 .Lca_slow_18

.Lk_298:
	s_and_b64 vcc, exec, s[0:1]
	s_cbranch_vccz .Lk_313
	s_setprio 3
	s_mul_i32 s68, s15, 0x1c2
	s_add_u32 s68, s68, s33
	s_add_u32 s68, s68, 66
	s_lshl_b32 s69, s68, 4
	s_add_u32 s70, s54, s69
	s_addc_u32 s71, s55, 0
	s_add_u32 s72, s70, 0xe100
	s_addc_u32 s73, s71, 0
	s_lshl_b32 s69, s68, 2
	s_add_u32 s74, s56, s69
	s_addc_u32 s75, s57, 0
	s_add_u32 s76, s74, 0x3840
	s_addc_u32 s77, s75, 0
	v_lshlrev_b32_e32 v60, 4, v80
	v_lshlrev_b32_e32 v61, 2, v80
	global_load_dwordx4 v[64:67], v60, s[70:71]
	global_load_dwordx4 v[68:71], v60, s[72:73]
	global_load_dword v72, v61, s[74:75]
	global_load_dword v73, v61, s[76:77]
	s_lshl_b32 s69, s15, 2
	v_lshlrev_b32_e32 v63, 6, v80
	v_add_u32_e32 v63, s69, v63
	v_add_u32_e32 v63, 0x1080, v63
	v_lshlrev_b32_e32 v62, 2, v63
	v_add_u32_e32 v63, 0x1c200, v63
	ds_read_b128 v[34:37], v81
	v_mov_b32_e32 v40, 0
	v_mov_b32_e32 v41, 0
	s_mov_b32 s0, 0x4038aa3b
	s_mov_b32 s1, 0
	v_mov_b32_e32 v58, 0xc038aa3b
	v_mov_b32_e32 v59, 0xc038aa3b
	v_mov_b32_e32 v39, v81
	s_mov_b32 s9, 2
	s_waitcnt lgkmcnt(0)
	ds_read_b128 v[42:45], v78 offset:2048
	ds_read_b128 v[46:49], v78 offset:3072
	v_mfma_f32_16x16x32_f16 v[50:53], v[2:5], v[34:37], v[6:9]
	v_mfma_f32_16x16x32_f16 v[54:57], v[26:29], v[34:37], v[30:33]
	s_waitcnt lgkmcnt(1)
	v_mfma_f32_16x16x32_f16 v[50:53], v[18:21], v[42:45], v[50:53]
	v_mfma_f32_16x16x32_f16 v[54:57], v[10:13], v[42:45], v[54:57]
	s_waitcnt lgkmcnt(0)
	v_mfma_f32_16x16x32_f16 v[50:53], v[22:25], v[46:49], v[50:53]
	v_mfma_f32_16x16x32_f16 v[54:57], v[14:17], v[46:49], v[54:57]
	ds_read_b128 v[34:37], v39 offset:256
	s_nop 6
	v_exp_f32_e32 v84, v52
	v_exp_f32_e32 v85, v56
	v_exp_f32_e32 v86, v50
	v_exp_f32_e32 v87, v54
	v_exp_f32_e32 v88, v51
	v_exp_f32_e32 v89, v55
	v_pk_add_f32 v[90:91], v[84:85], 1.0 op_sel_hi:[1,0]
	v_pk_fma_f32 v[92:93], v[84:85], s[0:1], v[58:59] op_sel_hi:[1,0,0]
	v_pk_fma_f32 v[90:91], v[86:87], v[90:91], v[90:91]
	v_pk_fma_f32 v[94:95], v[90:91], v[88:89], v[90:91]
	v_rcp_f32_e32 v94, v94
	v_rcp_f32_e32 v95, v95
	v_pk_fma_f32 v[92:93], v[92:93], v[88:89], v[92:93]
	v_pk_fma_f32 v[92:93], v[40:41], v[90:91], v[92:93]
	v_exp_f32_e32 v96, v53
	v_pk_mul_f32 v[40:41], v[92:93], v[94:95]
	v_exp_f32_e32 v98, v40
	v_exp_f32_e32 v99, v41
	v_exp_f32_e32 v97, v57
	v_pk_add_f32 v[100:101], v[98:99], 1.0 op_sel_hi:[1,0]
	v_pk_fma_f32 v[100:101], v[100:101], v[96:97], v[100:101]
	v_rcp_f32_e32 v100, v100
	v_rcp_f32_e32 v101, v101
	v_pk_add_f32 v[102:103], v[98:99], -1.0 op_sel_hi:[1,0]
	v_pk_mul_f32 v[102:103], v[102:103], v[100:101]
	v_cvt_pk_f16_f32 v104, v102, v103
	ds_write_b32 v79, v104 offset:0
	s_waitcnt lgkmcnt(0)
	s_barrier
	ds_read_b128 v[42:45], v78 offset:0
	ds_read_b128 v[46:49], v78 offset:1024
	v_mfma_f32_16x16x32_f16 v[50:53], v[2:5], v[34:37], v[6:9]
	v_mfma_f32_16x16x32_f16 v[54:57], v[26:29], v[34:37], v[30:33]
	s_waitcnt lgkmcnt(1)
	v_mfma_f32_16x16x32_f16 v[50:53], v[18:21], v[42:45], v[50:53]
	v_mfma_f32_16x16x32_f16 v[54:57], v[10:13], v[42:45], v[54:57]
	s_waitcnt lgkmcnt(0)
	v_mfma_f32_16x16x32_f16 v[50:53], v[22:25], v[46:49], v[50:53]
	v_mfma_f32_16x16x32_f16 v[54:57], v[14:17], v[46:49], v[54:57]
	ds_read_b128 v[34:37], v39 offset:512
	s_nop 6
	v_exp_f32_e32 v84, v52
	v_exp_f32_e32 v85, v56
	v_exp_f32_e32 v86, v50
	v_exp_f32_e32 v87, v54
	v_exp_f32_e32 v88, v51
	v_exp_f32_e32 v89, v55
	v_pk_add_f32 v[90:91], v[84:85], 1.0 op_sel_hi:[1,0]
	v_pk_fma_f32 v[92:93], v[84:85], s[0:1], v[58:59] op_sel_hi:[1,0,0]
	v_pk_fma_f32 v[90:91], v[86:87], v[90:91], v[90:91]
	v_pk_fma_f32 v[94:95], v[90:91], v[88:89], v[90:91]
	v_rcp_f32_e32 v94, v94
	v_rcp_f32_e32 v95, v95
	v_pk_fma_f32 v[92:93], v[92:93], v[88:89], v[92:93]
	v_pk_fma_f32 v[92:93], v[40:41], v[90:91], v[92:93]
	v_exp_f32_e32 v96, v53
	v_pk_mul_f32 v[40:41], v[92:93], v[94:95]
	v_exp_f32_e32 v98, v40
	v_exp_f32_e32 v99, v41
	v_exp_f32_e32 v97, v57
	v_pk_add_f32 v[100:101], v[98:99], 1.0 op_sel_hi:[1,0]
	v_pk_fma_f32 v[100:101], v[100:101], v[96:97], v[100:101]
	v_rcp_f32_e32 v100, v100
	v_rcp_f32_e32 v101, v101
	v_pk_add_f32 v[102:103], v[98:99], -1.0 op_sel_hi:[1,0]
	v_pk_mul_f32 v[102:103], v[102:103], v[100:101]
	v_cvt_pk_f16_f32 v104, v102, v103
	ds_write_b32 v79, v104 offset:2048
	s_waitcnt lgkmcnt(0)
	v_add_u32_e32 v39, 0x200, v39
	.p2align	6
